# c37: c29 + FINAL phase: the first pair-row loads (sunk by the compiler behind the slot-table test) are issued up front with the other loads - one memory round trip per pass instead of two
# speedup vs baseline: 1.0026x; 1.0011x over previous
; #define GAS __attribute__((address_space(1)))
; __global__ void __launch_bounds__(NTHREADS, 2) fwd(Args args) {
;     ...
;         for (int t0 = 2 * gw; t0 < SEQ; t0 += 2 * NGW) {
;             unsigned long long hr[2][4]; unsigned pr[2][2][4]; int sl[2][2];
; #pragma unroll
;             for (int r = 0; r < 2; ++r) { const int t = t0 + r;
;                 const GAS unsigned long long* hp = (const GAS unsigned long long*)(HN + (size_t)t * DM) + F.lane;
; #pragma unroll
;                 for (int q = 0; q < 4; ++q) hr[r][q] = __builtin_nontemporal_load(hp + 64 * q);
; #pragma unroll
;                 for (int k = 0; k < 2; ++k) { const GAS unsigned* pa = (const GAS unsigned*)((const unsigned char*)PAIR + (size_t)(2 * t + k) * DM) + F.lane;
; #pragma unroll
;                     for (int q = 0; q < 4; ++q) pr[r][k][q] = __builtin_nontemporal_load(pa + 64 * q);
;                     sl[r][k] = SLOTOF[2 * t + k]; } }
; #pragma unroll
;             for (int r = 0; r < 2; ++r) { const int t = t0 + r;
;                 f32x4 v[4];
; #pragma unroll
;                 for (int q = 0; q < 4; ++q) { const unsigned long long a = hr[r][q]; v[q] = (f32x4){bf2f((unsigned short)a), bf2f((unsigned short)(a >> 16)), bf2f((unsigned short)(a >> 32)), bf2f((unsigned short)(a >> 48))}; }
; #pragma unroll
;                 for (int k = 0; k < 2; ++k) { const int slot = sl[r][k];
;                     if ((slot >> 8) < 128) {
; #pragma unroll
;                         for (int q = 0; q < 4; ++q) { const unsigned a = pr[r][k][q];
;                             const auto lo = __builtin_amdgcn_cvt_pk_f32_fp8((int)a, false), hi = __builtin_amdgcn_cvt_pk_f32_fp8((int)a, true);
;                             v[q].x += lo[0] * 0.0625f; v[q].y += lo[1] * 0.0625f; v[q].z += hi[0] * 0.0625f; v[q].w += hi[1] * 0.0625f; }
;                     } else { const int lt = (slot >> 8) - 128, rl = slot & 255; const float gt = GATES[2 * t + k] * (1.0f / 32.0f);
; #pragma unroll
;                         for (int q = 0; q < 4; ++q) { const GAS f32x4* pp = (const GAS f32x4*)(PART + (size_t)((lt * 4 + q) * 7) * 65536 + rl * 256) + F.lane; f32x4 s = pp[0];
; #pragma unroll
;                             for (int s7 = 1; s7 < 7; ++s7) s += pp[(size_t)s7 * 16384];
;                             v[q] += s * gt; } } }
.LBB0_1479:
	s_ashr_i32 s5, s4, 31
	s_lshl_b64 s[42:43], s[4:5], 10
	v_lshl_add_u64 v[186:187], v[54:55], 0, s[42:43]
	global_load_dword v188, v[186:187], off nt
	global_load_dword v189, v[186:187], off offset:256 nt
	global_load_dword v190, v[186:187], off offset:512 nt
	global_load_dword v191, v[186:187], off offset:768 nt
	s_lshl_b64 s[16:17], s[4:5], 2
	s_add_u32 s18, s7, s16
	s_addc_u32 s19, s20, s17
	s_add_i32 s0, s4, 1
	s_ashr_i32 s1, s0, 31
	s_lshl_b64 s[12:13], s[0:1], 10
	s_lshl_b64 s[0:1], s[0:1], 2
	s_add_u32 s34, s7, s0
	v_lshl_add_u64 v[24:25], v[54:55], 0, s[12:13]
	s_addc_u32 s35, s20, s1
	s_add_i32 s12, s4, 2
	s_ashr_i32 s13, s12, 31
	s_lshl_b64 s[14:15], s[12:13], 10
	global_load_dwordx2 v[16:17], v[58:59], off nt
	global_load_dwordx2 v[18:19], v[58:59], off offset:512 nt
	global_load_dwordx2 v[20:21], v[58:59], off offset:1024 nt
	global_load_dwordx2 v[22:23], v[58:59], off offset:1536 nt
	global_load_dwordx2 v[66:67], v[58:59], off offset:2048 nt
	global_load_dwordx2 v[64:65], v[58:59], off offset:2560 nt
	global_load_dwordx2 v[62:63], v[58:59], off offset:3072 nt
	global_load_dwordx2 v[60:61], v[58:59], off offset:3584 nt
	v_lshl_add_u64 v[26:27], v[54:55], 0, s[14:15]
	global_load_dword v95, v[24:25], off nt
	global_load_dword v94, v[24:25], off offset:256 nt
	global_load_dword v93, v[24:25], off offset:512 nt
	global_load_dword v92, v[24:25], off offset:768 nt
	global_load_dword v91, v[26:27], off nt
	global_load_dword v90, v[26:27], off offset:256 nt
	global_load_dword v89, v[26:27], off offset:512 nt
	global_load_dword v88, v[26:27], off offset:768 nt
	s_lshl_b64 s[14:15], s[12:13], 2
	s_add_u32 s36, s7, s14
	s_addc_u32 s37, s20, s15
	s_add_i32 s12, s4, 3
	s_ashr_i32 s13, s12, 31
	s_lshl_b64 s[38:39], s[12:13], 10
	s_lshl_b64 s[12:13], s[12:13], 2
	v_lshl_add_u64 v[24:25], v[54:55], 0, s[38:39]
	s_add_u32 s38, s7, s12
	s_addc_u32 s39, s20, s13
	global_load_dword v26, v53, s[18:19]
	global_load_dword v27, v53, s[34:35]
	global_load_dword v28, v53, s[36:37]
	global_load_dword v87, v[24:25], off nt
	global_load_dword v86, v[24:25], off offset:256 nt
	global_load_dword v29, v53, s[38:39]
	global_load_dword v85, v[24:25], off offset:512 nt
	global_load_dword v84, v[24:25], off offset:768 nt
	s_mov_b64 s[18:19], -1
	v_lshlrev_b32_e32 v52, 4, v162
	s_waitcnt vmcnt(23)
	v_lshlrev_b32_e32 v44, 16, v16
	v_and_b32_e32 v45, 0xffff0000, v16
	v_alignbit_b32 v16, v17, v16, 16
	v_and_b32_e32 v47, 0xffff0000, v17
	s_waitcnt vmcnt(22)
	v_lshlrev_b32_e32 v48, 16, v18
	v_and_b32_e32 v49, 0xffff0000, v18
	v_alignbit_b32 v17, v19, v18, 16
	v_and_b32_e32 v51, 0xffff0000, v19
	s_waitcnt vmcnt(21)
	v_alignbit_b32 v18, v21, v20, 16
	s_waitcnt vmcnt(20)
	v_alignbit_b32 v19, v23, v22, 16
	s_waitcnt vmcnt(7)
	v_readfirstlane_b32 s37, v26
	s_ashr_i32 s2, s37, 8
	v_lshlrev_b32_e32 v70, 16, v20
	v_and_b32_e32 v71, 0xffff0000, v20
	v_and_b32_e32 v73, 0xffff0000, v21
	v_lshlrev_b32_e32 v68, 16, v22
	v_and_b32_e32 v69, 0xffff0000, v22
	v_and_b32_e32 v75, 0xffff0000, v23
	v_and_b32_e32 v46, 0xffff0000, v16
	v_and_b32_e32 v50, 0xffff0000, v17
	v_and_b32_e32 v72, 0xffff0000, v18
	v_and_b32_e32 v74, 0xffff0000, v19
	s_cmpk_gt_i32 s2, 0x7f
	s_waitcnt vmcnt(6)
	v_readfirstlane_b32 s36, v27
	s_waitcnt vmcnt(5)
	v_readfirstlane_b32 s35, v28
	s_waitcnt vmcnt(2)
	v_readfirstlane_b32 s34, v29
	s_cbranch_scc0 .LBB0_1481
	s_add_u32 s38, s21, s16
	s_addc_u32 s39, s22, s17
	s_lshl_b32 s16, s37, 10
	s_and_b32 s16, s16, 0x3fc00
	s_add_u32 s16, s23, s16
	s_mul_i32 s18, s2, 28
	s_addc_u32 s17, s24, 0
	s_add_i32 s2, s18, 0xfffff200
	s_lshl_b64 s[40:41], s[2:3], 18
	s_add_u32 s40, s16, s40
	s_addc_u32 s41, s17, s41
	v_lshl_add_u64 v[36:37], s[40:41], 0, v[52:53]
	v_add_co_u32_e32 v28, vcc, s26, v36
	s_add_i32 s2, s18, 0xfffff207
	s_nop 0
	v_addc_co_u32_e32 v29, vcc, 0, v37, vcc
	v_add_co_u32_e32 v30, vcc, s27, v36
	global_load_dword v163, v53, s[38:39]
	global_load_dwordx4 v[16:19], v52, s[40:41]
	v_addc_co_u32_e32 v31, vcc, 0, v37, vcc
	v_add_co_u32_e32 v38, vcc, s28, v36
	s_lshl_b64 s[38:39], s[2:3], 18
	s_nop 0
	v_addc_co_u32_e32 v39, vcc, 0, v37, vcc
	v_add_co_u32_e32 v40, vcc, s29, v36
	s_add_u32 s38, s16, s38
	s_nop 0
	v_addc_co_u32_e32 v41, vcc, 0, v37, vcc
	v_add_co_u32_e32 v96, vcc, s30, v36
	s_addc_u32 s39, s17, s39
	s_nop 0
	v_addc_co_u32_e32 v97, vcc, 0, v37, vcc
	v_add_co_u32_e32 v98, vcc, s31, v36
	v_lshl_add_u64 v[112:113], s[38:39], 0, v[52:53]
	s_nop 0
	v_addc_co_u32_e32 v99, vcc, 0, v37, vcc
	v_add_co_u32_e32 v104, vcc, s26, v112
	s_add_i32 s2, s18, 0xfffff20e
	s_nop 0
	v_addc_co_u32_e32 v105, vcc, 0, v113, vcc
	v_add_co_u32_e32 v106, vcc, s27, v112
	s_lshl_b64 s[40:41], s[2:3], 18
	s_nop 0
	v_addc_co_u32_e32 v107, vcc, 0, v113, vcc
	v_add_co_u32_e32 v114, vcc, s28, v112
	s_add_u32 s40, s16, s40
	s_nop 0
	v_addc_co_u32_e32 v115, vcc, 0, v113, vcc
	v_add_co_u32_e32 v116, vcc, s29, v112
	s_addc_u32 s41, s17, s41
	s_nop 0
	v_addc_co_u32_e32 v117, vcc, 0, v113, vcc
	v_add_co_u32_e32 v120, vcc, s30, v112
	v_lshl_add_u64 v[144:145], s[40:41], 0, v[52:53]
	s_nop 0
	v_addc_co_u32_e32 v121, vcc, 0, v113, vcc
	v_add_co_u32_e32 v122, vcc, s31, v112
	s_add_i32 s2, s18, 0xfffff215
	s_nop 0
	v_addc_co_u32_e32 v123, vcc, 0, v113, vcc
	v_add_co_u32_e32 v128, vcc, s26, v144
	global_load_dwordx4 v[20:23], v[28:29], off
	global_load_dwordx4 v[24:27], v[30:31], off
	v_addc_co_u32_e32 v129, vcc, 0, v145, vcc
	v_add_co_u32_e32 v132, vcc, s27, v144
	global_load_dwordx4 v[28:31], v[38:39], off
	global_load_dwordx4 v[32:35], v[40:41], off
	v_addc_co_u32_e32 v133, vcc, 0, v145, vcc
	v_add_co_u32_e32 v136, vcc, s28, v144
	global_load_dwordx4 v[36:39], v[96:97], off
	global_load_dwordx4 v[40:43], v[98:99], off
	v_addc_co_u32_e32 v137, vcc, 0, v145, vcc
	v_add_co_u32_e32 v140, vcc, s29, v144
	global_load_dwordx4 v[96:99], v[104:105], off
	global_load_dwordx4 v[100:103], v[106:107], off
	v_addc_co_u32_e32 v141, vcc, 0, v145, vcc
	global_load_dwordx4 v[104:107], v[114:115], off
	global_load_dwordx4 v[108:111], v[116:117], off
	s_nop 0
	global_load_dwordx4 v[112:115], v[120:121], off
	global_load_dwordx4 v[116:119], v[122:123], off
	s_nop 0
	global_load_dwordx4 v[120:123], v52, s[38:39]
	global_load_dwordx4 v[124:127], v52, s[40:41]
	v_add_co_u32_e32 v146, vcc, s30, v144
	s_lshl_b64 s[18:19], s[2:3], 18
	s_waitcnt lgkmcnt(0)
; #define GAS __attribute__((address_space(1)))
; __global__ void __launch_bounds__(NTHREADS, 2) fwd(Args args) {
;     ...
;                     } else { const int lt = (slot >> 8) - 128, rl = slot & 255; const float gt = GATES[2 * t + k] * (1.0f / 32.0f);
; #pragma unroll
;                         for (int q = 0; q < 4; ++q) { const GAS f32x4* pp = (const GAS f32x4*)(PART + (size_t)((lt * 4 + q) * 7) * 65536 + rl * 256) + F.lane; f32x4 s = pp[0];
; #pragma unroll
;                             for (int s7 = 1; s7 < 7; ++s7) s += pp[(size_t)s7 * 16384];
;                             v[q] += s * gt; } } }
	v_addc_co_u32_e32 v147, vcc, 0, v145, vcc
	s_add_u32 s16, s16, s18
	v_add_co_u32_e32 v148, vcc, s31, v144
	s_addc_u32 s17, s17, s19
	s_nop 0
	v_addc_co_u32_e32 v149, vcc, 0, v145, vcc
	v_lshl_add_u64 v[160:161], s[16:17], 0, v[52:53]
	v_add_co_u32_e32 v156, vcc, s26, v160
	global_load_dwordx4 v[128:131], v[128:129], off
	s_nop 0
	global_load_dwordx4 v[132:135], v[132:133], off
	v_addc_co_u32_e32 v157, vcc, 0, v161, vcc
	v_add_co_u32_e32 v164, vcc, s27, v160
	global_load_dwordx4 v[136:139], v[136:137], off
	s_nop 0
	global_load_dwordx4 v[140:143], v[140:141], off
	v_addc_co_u32_e32 v165, vcc, 0, v161, vcc
	v_add_co_u32_e32 v168, vcc, s28, v160
	global_load_dwordx4 v[144:147], v[146:147], off
	s_nop 0
	global_load_dwordx4 v[148:151], v[148:149], off
	v_addc_co_u32_e32 v169, vcc, 0, v161, vcc
	v_add_co_u32_e32 v172, vcc, s29, v160
	global_load_dwordx4 v[152:155], v52, s[16:17]
	s_nop 0
	v_addc_co_u32_e32 v173, vcc, 0, v161, vcc
	global_load_dwordx4 v[156:159], v[156:157], off
	s_nop 0
	global_load_dwordx4 v[164:167], v[164:165], off
	v_add_co_u32_e32 v176, vcc, s30, v160
	global_load_dwordx4 v[168:171], v[168:169], off
	s_nop 0
	global_load_dwordx4 v[172:175], v[172:173], off
	v_addc_co_u32_e32 v177, vcc, 0, v161, vcc
	v_add_co_u32_e32 v160, vcc, 0x180000, v160
	global_load_dwordx4 v[176:179], v[176:177], off
	s_nop 0
	v_addc_co_u32_e32 v161, vcc, 0, v161, vcc
	global_load_dwordx4 v[180:183], v[160:161], off
	s_waitcnt vmcnt(28)
	v_mul_f32_e32 v160, 0x3d000000, v163
	s_waitcnt vmcnt(26)
	v_pk_add_f32 v[18:19], v[18:19], v[22:23]
	v_pk_add_f32 v[16:17], v[16:17], v[20:21]
	s_waitcnt vmcnt(25)
	v_pk_add_f32 v[18:19], v[18:19], v[26:27]
	v_pk_add_f32 v[16:17], v[16:17], v[24:25]
	s_waitcnt vmcnt(24)
	v_pk_add_f32 v[18:19], v[18:19], v[30:31]
	v_pk_add_f32 v[16:17], v[16:17], v[28:29]
	s_waitcnt vmcnt(23)
	v_pk_add_f32 v[18:19], v[18:19], v[34:35]
	v_pk_add_f32 v[16:17], v[16:17], v[32:33]
	s_waitcnt vmcnt(22)
	v_pk_add_f32 v[18:19], v[18:19], v[38:39]
	v_pk_add_f32 v[16:17], v[16:17], v[36:37]
	s_waitcnt vmcnt(21)
	v_pk_add_f32 v[18:19], v[18:19], v[42:43]
	v_pk_add_f32 v[16:17], v[16:17], v[40:41]
	v_pk_fma_f32 v[18:19], v[160:161], v[18:19], v[46:47] op_sel_hi:[0,1,1]
	v_pk_fma_f32 v[16:17], v[160:161], v[16:17], v[44:45] op_sel_hi:[0,1,1]
	s_waitcnt vmcnt(14)
	v_pk_add_f32 v[20:21], v[122:123], v[98:99]
	v_pk_add_f32 v[22:23], v[120:121], v[96:97]
	v_pk_add_f32 v[20:21], v[20:21], v[102:103]
	v_pk_add_f32 v[22:23], v[22:23], v[100:101]
	v_pk_add_f32 v[20:21], v[20:21], v[106:107]
	v_pk_add_f32 v[22:23], v[22:23], v[104:105]
	v_pk_add_f32 v[20:21], v[20:21], v[110:111]
	v_pk_add_f32 v[22:23], v[22:23], v[108:109]
	v_pk_add_f32 v[20:21], v[20:21], v[114:115]
	v_pk_add_f32 v[22:23], v[22:23], v[112:113]
	v_pk_add_f32 v[20:21], v[20:21], v[118:119]
	v_pk_add_f32 v[24:25], v[22:23], v[116:117]
	v_pk_fma_f32 v[22:23], v[160:161], v[20:21], v[50:51] op_sel_hi:[0,1,1]
	v_pk_fma_f32 v[20:21], v[160:161], v[24:25], v[48:49] op_sel_hi:[0,1,1]
	s_waitcnt vmcnt(12)
	v_pk_add_f32 v[24:25], v[126:127], v[130:131]
	v_pk_add_f32 v[26:27], v[124:125], v[128:129]
	s_waitcnt vmcnt(11)
	v_pk_add_f32 v[24:25], v[24:25], v[134:135]
	v_pk_add_f32 v[26:27], v[26:27], v[132:133]
	s_waitcnt vmcnt(10)
	v_pk_add_f32 v[24:25], v[24:25], v[138:139]
	v_pk_add_f32 v[26:27], v[26:27], v[136:137]
	s_waitcnt vmcnt(9)
	v_pk_add_f32 v[24:25], v[24:25], v[142:143]
	v_pk_add_f32 v[26:27], v[26:27], v[140:141]
	s_waitcnt vmcnt(8)
	v_pk_add_f32 v[24:25], v[24:25], v[146:147]
	v_pk_add_f32 v[26:27], v[26:27], v[144:145]
	s_waitcnt vmcnt(7)
	v_pk_add_f32 v[24:25], v[24:25], v[150:151]
	v_pk_add_f32 v[28:29], v[26:27], v[148:149]
	v_pk_fma_f32 v[26:27], v[160:161], v[24:25], v[72:73] op_sel_hi:[0,1,1]
	v_pk_fma_f32 v[24:25], v[160:161], v[28:29], v[70:71] op_sel_hi:[0,1,1]
	s_waitcnt vmcnt(5)
	v_pk_add_f32 v[28:29], v[154:155], v[158:159]
	v_pk_add_f32 v[30:31], v[152:153], v[156:157]
	s_waitcnt vmcnt(4)
	v_pk_add_f32 v[28:29], v[28:29], v[166:167]
	v_pk_add_f32 v[30:31], v[30:31], v[164:165]
	s_waitcnt vmcnt(3)
	v_pk_add_f32 v[28:29], v[28:29], v[170:171]
	v_pk_add_f32 v[30:31], v[30:31], v[168:169]
	s_waitcnt vmcnt(2)
	v_pk_add_f32 v[28:29], v[28:29], v[174:175]
	v_pk_add_f32 v[30:31], v[30:31], v[172:173]
	s_waitcnt vmcnt(1)
	v_pk_add_f32 v[28:29], v[28:29], v[178:179]
	v_pk_add_f32 v[30:31], v[30:31], v[176:177]
	s_waitcnt vmcnt(0)
	v_pk_add_f32 v[28:29], v[28:29], v[182:183]
	v_pk_add_f32 v[32:33], v[30:31], v[180:181]
	v_pk_fma_f32 v[30:31], v[160:161], v[28:29], v[74:75] op_sel_hi:[0,1,1]
	v_pk_fma_f32 v[28:29], v[160:161], v[32:33], v[68:69] op_sel_hi:[0,1,1]
	s_cbranch_execnz .LBB0_1483
	s_branch .LBB0_1482

; __global__ void __launch_bounds__(NTHREADS, 2) fwd(Args args) {
;     ...
;                     if ((slot >> 8) < 128) {
; #pragma unroll
;                         for (int q = 0; q < 4; ++q) { const unsigned a = pr[r][k][q];
;                             const auto lo = __builtin_amdgcn_cvt_pk_f32_fp8((int)a, false), hi = __builtin_amdgcn_cvt_pk_f32_fp8((int)a, true);
;                             v[q].x += lo[0] * 0.0625f; v[q].y += lo[1] * 0.0625f; v[q].z += hi[0] * 0.0625f; v[q].w += hi[1] * 0.0625f; }
.LBB0_1482:
	s_lshl_b64 s[16:17], s[4:5], 10
	v_lshl_add_u64 v[16:17], v[54:55], 0, s[16:17]
	v_cvt_pk_f32_fp8_e32 v[16:17], v188
	v_cvt_pk_f32_fp8_sdwa v[18:19], v188 src0_sel:WORD_1
	v_cvt_pk_f32_fp8_e32 v[20:21], v189
	v_cvt_pk_f32_fp8_sdwa v[22:23], v189 src0_sel:WORD_1
	v_cvt_pk_f32_fp8_e32 v[24:25], v190
	v_cvt_pk_f32_fp8_sdwa v[26:27], v190 src0_sel:WORD_1
	v_cvt_pk_f32_fp8_e32 v[28:29], v191
	v_cvt_pk_f32_fp8_sdwa v[30:31], v191 src0_sel:WORD_1
	v_pk_fma_f32 v[16:17], v[16:17], s[6:7], v[44:45] op_sel_hi:[1,0,1]
	v_pk_fma_f32 v[18:19], v[18:19], s[6:7], v[46:47] op_sel_hi:[1,0,1]
	v_pk_fma_f32 v[20:21], v[20:21], s[6:7], v[48:49] op_sel_hi:[1,0,1]
	v_pk_fma_f32 v[22:23], v[22:23], s[6:7], v[50:51] op_sel_hi:[1,0,1]
	v_pk_fma_f32 v[24:25], v[24:25], s[6:7], v[70:71] op_sel_hi:[1,0,1]
	v_pk_fma_f32 v[26:27], v[26:27], s[6:7], v[72:73] op_sel_hi:[1,0,1]
	v_pk_fma_f32 v[28:29], v[28:29], s[6:7], v[68:69] op_sel_hi:[1,0,1]
	v_pk_fma_f32 v[30:31], v[30:31], s[6:7], v[74:75] op_sel_hi:[1,0,1]
